# speedup vs baseline: 1.0113x; 1.0113x over previous
.LBB1_2:
	s_load_dwordx8 s[4:11], s[0:1], 0x0
	s_lshr_b32 s0, s2, 3
	s_bfe_u32 s33, s2, 0x30003
	v_readfirstlane_b32 s36, v0
	s_and_b32 s3, s2, 7
	s_and_b32 s0, s0, 8
	s_xor_b32 s44, s33, 15
	s_bfe_u32 s38, s36, 0x20006
	s_or_b32 s14, s0, s3
	s_lshr_b32 s30, s2, 7
	s_mov_b32 s31, 0
	s_lshl_b32 s0, s44, 7
	s_lshl_b32 s39, s38, 5
	s_lshl_b64 s[18:19], s[30:31], 11
	s_or_b32 s0, s39, s0
	s_or_b32 s0, s18, s0
	s_mov_b32 s1, s19
	s_lshr_b32 s35, s36, 6
	s_lshr_b32 s37, s36, 8
	s_lshl_b64 s[12:13], s[0:1], 11
	s_waitcnt lgkmcnt(0)
	s_add_u32 s12, s4, s12
	s_addc_u32 s13, s5, s13
	s_lshl_b32 s42, s14, 6
	s_lshl_b32 s14, s14, 7
	s_add_u32 s16, s12, s14
	s_addc_u32 s17, s13, 0
	s_lshl_b64 s[12:13], s[30:31], 22
	s_add_u32 s6, s6, s12
	s_addc_u32 s7, s7, s13
	s_add_u32 s6, s6, s14
	s_addc_u32 s7, s7, 0
	s_lshr_b32 s15, s36, 4
	v_and_b32_e32 v200, 7, v0
	v_bfe_u32 v208, v0, 4, 2
	s_and_b32 s15, s15, 4
	v_bfe_u32 v193, v0, 3, 3
	v_bitop3_b32 v1, s15, v200, v208 bitop3:0x36
	s_add_u32 s15, s8, s12
	v_lshl_or_b32 v188, s35, 3, v193
	v_mov_b32_e32 v189, 0
	s_addc_u32 s20, s9, s13
	v_lshlrev_b64 v[2:3], 11, v[188:189]
	v_lshlrev_b32_e32 v188, 4, v1
	s_add_u32 s14, s15, s14
	v_lshlrev_b32_e32 v1, 8, v0
	v_lshl_add_u64 v[2:3], s[6:7], 0, v[2:3]
	s_addc_u32 s15, s20, 0
	s_lshl_b32 s34, s38, 14
	v_and_b32_e32 v1, 0x3c00, v1
	v_lshl_add_u64 v[194:195], v[2:3], 0, v[188:189]
	v_or_b32_e32 v2, s34, v1
	s_lshl_b32 s30, s37, 6
	s_lshl_b32 s20, s35, 10
	v_lshlrev_b32_e32 v188, 1, v2
	v_lshlrev_b32_e32 v4, 3, v0
	s_cmp_lg_u32 0, -1
	v_lshl_add_u64 v[2:3], s[14:15], 0, v[188:189]
	v_and_b32_e32 v209, 24, v4
	s_cselect_b32 s21, 0, 0
	v_lshl_add_u64 v[2:3], v[2:3], 0, s[30:31]
	v_lshlrev_b32_e32 v190, 1, v209
	v_mov_b32_e32 v191, v189
	s_add_i32 s41, s20, s21
	s_mov_b32 s21, m0
	s_mov_b32 m0, s41
	s_nop 0
	global_load_lds_dwordx4 v[194:195], off
	s_mov_b32 m0, s21
	s_mov_b64 s[22:23], 0x20000
	v_lshl_add_u64 v[196:197], v[2:3], 0, v[190:191]
	v_lshl_add_u64 v[2:3], v[194:195], 0, s[22:23]
	s_add_i32 s21, s41, 0x2000
	s_mov_b32 s24, m0
	s_mov_b32 m0, s21
	s_nop 0
	global_load_lds_dwordx4 v[2:3], off
	s_mov_b32 m0, s24
	v_and_b32_e32 v202, 31, v0
	v_bfe_u32 v201, v0, 5, 1
	v_lshlrev_b32_e32 v216, 10, v202
	v_lshl_or_b32 v216, v201, 3, v216
	v_lshlrev_b32_e32 v216, 1, v216
	global_load_dwordx4 v[144:147], v216, s[16:17]
	global_load_dwordx4 v[140:143], v216, s[16:17] offset:32
	global_load_dwordx4 v[136:139], v216, s[16:17] offset:64
	global_load_dwordx4 v[132:135], v216, s[16:17] offset:96
	s_add_i32 s40, s41, 0xc000
	s_mov_b32 s24, m0
	s_mov_b32 m0, s40
	s_nop 0
	global_load_lds_dwordx4 v[196:197], off
	s_mov_b32 m0, s24
	v_lshl_add_u64 v[198:199], v[196:197], 0, s[22:23]
	s_add_i32 s24, s40, 0x2000
	s_mov_b32 s25, m0
	s_mov_b32 m0, s24
	s_nop 0
	global_load_lds_dwordx4 v[198:199], off
	s_mov_b32 m0, s25
	s_mov_b64 s[24:25], 0x40000
	v_lshl_add_u64 v[2:3], v[194:195], 0, s[24:25]
	s_add_i32 s26, s41, 0x4000
	s_mov_b32 s27, m0
	s_mov_b32 m0, s26
	s_nop 0
	global_load_lds_dwordx4 v[2:3], off
	s_mov_b32 m0, s27
	s_mov_b64 s[26:27], 0x60000
	v_lshl_add_u64 v[2:3], v[194:195], 0, s[26:27]
	s_add_i32 s28, s41, 0x6000
	s_mov_b32 s29, m0
	s_mov_b32 m0, s28
	s_nop 0
	global_load_lds_dwordx4 v[2:3], off
	s_mov_b32 m0, s29
	s_lshl_b32 s28, s37, 13
	v_lshrrev_b32_e32 v2, 1, v0
	s_add_i32 s30, s28, 0
	v_bitop3_b32 v2, v201, v2, 7 bitop3:0x78
	s_mov_b64 s[28:29], 0x80000
	v_lshlrev_b32_e32 v207, 4, v2
	v_lshl_add_u64 v[2:3], v[194:195], 0, s[28:29]
	s_add_i32 s16, s41, 0x8000
	s_mov_b32 s17, m0
	s_mov_b32 m0, s16
	s_nop 0
	global_load_lds_dwordx4 v[2:3], off
	s_mov_b32 m0, s17
	v_lshlrev_b32_e32 v211, 7, v202
	s_mov_b64 s[16:17], 0xa0000
	v_add_u32_e32 v217, s30, v211
	v_lshl_add_u64 v[2:3], v[194:195], 0, s[16:17]
	s_add_i32 s16, s41, 0xa000
	s_mov_b32 s17, m0
	s_mov_b32 m0, s16
	s_nop 0
	global_load_lds_dwordx4 v[2:3], off
	s_mov_b32 m0, s17
	s_waitcnt vmcnt(6) lgkmcnt(0)
	s_barrier
	v_add_u32_e32 v70, v217, v207
	ds_read_b128 v[2:5], v70
	ds_read_b128 v[18:21], v70 offset:4096
	v_xor_b32_e32 v206, 32, v207
	v_add_u32_e32 v71, v217, v206
	ds_read_b128 v[22:25], v71
	ds_read_b128 v[34:37], v71 offset:4096
	v_xor_b32_e32 v205, 64, v207
	s_waitcnt lgkmcnt(3)
	v_mfma_f32_32x32x16_f16 v[2:17], v[2:5], v[144:147], 0
	v_add_u32_e32 v72, v217, v205
	v_xor_b32_e32 v204, 0x60, v207
	v_add_u32_e32 v73, v217, v204
	s_mov_b32 s46, 5
	s_movk_i32 s48, 0x4000
	s_mov_b32 s45, 0x8000
	v_and_b32_e32 v212, 63, v0
	s_waitcnt lgkmcnt(1)
	v_mfma_f32_32x32x16_f16 v[2:17], v[22:25], v[140:143], v[2:17]
	v_mfma_f32_32x32x16_f16 v[18:33], v[18:21], v[144:147], 0
	s_waitcnt lgkmcnt(0)
	v_mfma_f32_32x32x16_f16 v[18:33], v[34:37], v[140:143], v[18:33]
	ds_read_b128 v[34:37], v72
	ds_read_b128 v[38:41], v72 offset:4096
	s_waitcnt lgkmcnt(1)
	v_mfma_f32_32x32x16_f16 v[2:17], v[34:37], v[136:139], v[2:17]
	s_waitcnt lgkmcnt(0)
	v_mfma_f32_32x32x16_f16 v[18:33], v[38:41], v[136:139], v[18:33]
	ds_read_b128 v[34:37], v73
	ds_read_b128 v[38:41], v73 offset:4096
	s_waitcnt lgkmcnt(1)
	v_mfma_f32_32x32x16_f16 v[2:17], v[34:37], v[132:135], v[2:17]
	s_waitcnt lgkmcnt(0)
	v_mfma_f32_32x32x16_f16 v[18:33], v[38:41], v[132:135], v[18:33]
	s_nop 9
	v_max_f32_e64 v35, |v2|, |v2|
	s_nop 0
	v_max_f32_e64 v34, |v18|, |v18|
	v_min_f32_e32 v34, v35, v34
	v_min3_f32 v34, v34, |v3|, |v19|
	v_min3_f32 v34, v34, |v4|, |v20|
	v_min3_f32 v34, v34, |v5|, |v21|
	v_min3_f32 v34, v34, |v6|, |v22|
	v_min3_f32 v34, v34, |v7|, |v23|
	v_min3_f32 v34, v34, |v8|, |v24|
	v_min3_f32 v34, v34, |v9|, |v25|
	v_min3_f32 v34, v34, |v10|, |v26|
	v_min3_f32 v34, v34, |v11|, |v27|
	v_min3_f32 v34, v34, |v12|, |v28|
	v_min3_f32 v34, v34, |v13|, |v29|
	v_min3_f32 v34, v34, |v14|, |v30|
	v_min3_f32 v34, v34, |v15|, |v31|
	v_min3_f32 v34, v34, |v16|, |v32|
	v_min3_f32 v34, v34, |v17|, |v33|
	v_cmp_eq_f32_e32 vcc, 0, v34
	s_cbranch_vccnz .LBB1_114
